# peersel: query fragments of the next unit prefetched into a spare register set during the sort phase
# speedup vs baseline: 1.0240x; 1.0114x over previous
; DI int tidx() { int t = threadIdx.x & 255; asm volatile("" : "+v"(t)); return t; }
; DI void peer_select_unit(const Params& p, int unit, char* lds, const bf16x8 (&kb)[4][4]) {
;     ...
;     const int set = wid >> 1, kh = wid & 1;
;     bf16x8 qa[2][4];
; #pragma unroll
;     for (int mt = 0; mt < 2; ++mt)
; #pragma unroll
;       for (int kk = 0; kk < 4; ++kk) qa[mt][kk] = *(const bf16x8*)(qy + (size_t)(t0 + 16 * mt + fr) * 2048 + h * 256 + set * 128 + kk * 32 + fq * 8);
; DI void phase_peersel(const Params& p, int bid, int nb, char* lds) {
;   const int lane = tidx() & 63, wid = tidx() >> 6, fr = lane & 15, fq = lane >> 4;
;   const bf16_t* keys = (const bf16_t*)(p.ws + WS_KEYS) + (wid >> 1) * 16384 + (wid & 1) * 64 * 128;
;   bf16x8 kb[4][4];
; #pragma unroll
;   for (int nj = 0; nj < 4; ++nj)
; #pragma unroll
;     for (int kk = 0; kk < 4; ++kk) kb[nj][kk] = *(const bf16x8*)(keys + (16 * nj + fr) * 128 + kk * 32 + fq * 8);
;   for (int u = bid; u < 8192; u += nb) peer_select_unit(p, u, lds, kb);
.LBB0_1648:
	s_or_b64 exec, exec, s[0:1]
	s_movk_i32 s0, 0x2000
	s_waitcnt lgkmcnt(0)
	v_mov_b32_e32 v0, v206
	v_mov_b32_e32 v1, v206
	v_cmp_gt_i32_e32 vcc, s0, v176
	s_barrier
	s_and_saveexec_b64 s[52:53], vcc
	s_cbranch_execz .LBB0_1683
	v_lshlrev_b32_e32 v2, 7, v1
	v_and_b32_e32 v2, 0xffffc000, v2
	v_readlane_b32 s2, v250, 7
	v_ashrrev_i32_e32 v3, 31, v2
	v_readlane_b32 s3, v250, 8
	v_lshlrev_b32_e32 v1, 8, v1
	v_and_b32_e32 v64, 0x4000, v1
	v_lshl_add_u64 v[2:3], v[2:3], 1, s[2:3]
	v_mov_b32_e32 v65, 0
	v_lshl_add_u64 v[2:3], v[2:3], 0, v[64:65]
	v_and_b32_e32 v64, 48, v0
	v_lshlrev_b32_e32 v0, 8, v0
	v_lshl_add_u64 v[2:3], v[2:3], 0, v[64:65]
	v_and_b32_e32 v64, 0xf00, v0
	v_lshl_add_u64 v[40:41], v[2:3], 0, v[64:65]
	s_movk_i32 s1, 0x1000
	v_add_co_u32_e32 v66, vcc, s1, v40
	global_load_dwordx4 v[0:3], v[40:41], off
	global_load_dwordx4 v[4:7], v[40:41], off offset:64
	global_load_dwordx4 v[8:11], v[40:41], off offset:128
	global_load_dwordx4 v[12:15], v[40:41], off offset:192
	v_addc_co_u32_e32 v67, vcc, 0, v41, vcc
	v_add_co_u32_e32 v68, vcc, s0, v40
	s_movk_i32 s0, 0x3000
	s_nop 0
	v_addc_co_u32_e32 v69, vcc, 0, v41, vcc
	v_add_co_u32_e32 v70, vcc, s0, v40
	global_load_dwordx4 v[16:19], v[66:67], off offset:64
	global_load_dwordx4 v[20:23], v[66:67], off offset:128
	global_load_dwordx4 v[24:27], v[68:69], off
	global_load_dwordx4 v[28:31], v[68:69], off offset:64
	global_load_dwordx4 v[32:35], v[68:69], off offset:128
	global_load_dwordx4 v[36:39], v[68:69], off offset:192
	v_addc_co_u32_e32 v71, vcc, 0, v41, vcc
	global_load_dwordx4 v[40:43], v[66:67], off offset:192
	global_load_dwordx4 v[44:47], v[70:71], off
	global_load_dwordx4 v[48:51], v[70:71], off offset:64
	global_load_dwordx4 v[52:55], v[70:71], off offset:128
	global_load_dwordx4 v[56:59], v[68:69], off offset:-4096
	global_load_dwordx4 v[60:63], v[70:71], off offset:192
	s_add_u32 s60, s84, 0x12000000
	s_addc_u32 s61, s85, 0
	s_add_u32 s62, s84, 0x13000000
	s_addc_u32 s63, s85, 0
	s_mov_b64 s[64:65], 0
	s_movk_i32 s2, 0x210
	s_movk_i32 s3, 0x7f
	s_movk_i32 s18, 0x80
	s_movk_i32 s19, 0xff
	s_movk_i32 s68, 0x1fff
	v_mov_b32_e32 v72, v176
	v_and_b32_e32 v182, 15, v206
	v_lshlrev_b32_e32 v182, 12, v182
	v_bfe_u32 v183, v206, 4, 2
	v_lshl_or_b32 v182, v183, 4, v182
	v_lshrrev_b32_e32 v183, 7, v206
	v_lshl_or_b32 v182, v183, 8, v182
	v_mov_b32_e32 v183, 0
	v_lshl_add_u64 v[182:183], s[58:59], 0, v[182:183]
	v_mov_b32_e32 v184, v72
	v_lshrrev_b32_e32 v185, 3, v184
	v_lshlrev_b32_e32 v185, 17, v185
	v_and_b32_e32 v184, 7, v184
	v_lshl_or_b32 v184, v184, 9, v185
	v_mov_b32_e32 v185, 0
	v_lshl_add_u64 v[184:185], v[182:183], 0, v[184:185]
	v_mov_b32_e32 v186, 0x10000
	v_mov_b32_e32 v187, 0
	v_lshl_add_u64 v[186:187], v[184:185], 0, v[186:187]
	global_load_dwordx4 v[148:151], v[184:185], off
	global_load_dwordx4 v[152:155], v[184:185], off offset:64
	global_load_dwordx4 v[156:159], v[186:187], off
	global_load_dwordx4 v[160:163], v[186:187], off offset:64
	global_load_dwordx4 v[164:167], v[184:185], off offset:128
	global_load_dwordx4 v[168:171], v[184:185], off offset:192
	global_load_dwordx4 v[172:175], v[186:187], off offset:128
	global_load_dwordx4 v[178:181], v[186:187], off offset:192
	s_branch .LBB0_1652

; #define MFMA16(a, b, c) __builtin_amdgcn_mfma_f32_16x16x32_bf16((a), (b), (c), 0, 0, 0)
; DI void peer_select_unit(const Params& p, int unit, char* lds, const bf16x8 (&kb)[4][4]) {
;     ...
;   __syncthreads();
;   {
;     const int set = wid >> 1, kh = wid & 1;
;     bf16x8 qa[2][4];
; #pragma unroll
;     for (int mt = 0; mt < 2; ++mt)
; #pragma unroll
;       for (int kk = 0; kk < 4; ++kk) qa[mt][kk] = *(const bf16x8*)(qy + (size_t)(t0 + 16 * mt + fr) * 2048 + h * 256 + set * 128 + kk * 32 + fq * 8);
; #pragma unroll
;     for (int mt = 0; mt < 2; ++mt)
; #pragma unroll
;       for (int nj = 0; nj < 4; ++nj) {
;         f32x4 d = {0.f, 0.f, 0.f, 0.f};
; #pragma unroll
;         for (int kk = 0; kk < 4; ++kk) d = MFMA16(qa[mt][kk], kb[nj][kk], d);
; #pragma unroll
;         for (int r = 0; r < 4; ++r) sc[(set * 32 + 16 * mt + 4 * fq + r) * 132 + 64 * kh + 16 * nj + fr] = d[r];
;       }
;   }
.LBB0_1652:
	v_lshlrev_b32_e32 v64, 2, v72
	v_mov_b32_e32 v66, v206
	v_and_b32_e32 v73, 7, v72
	v_and_b32_e32 v74, 0xffffffe0, v64
	v_lshlrev_b32_e32 v64, 9, v73
	v_and_or_b32 v84, v66, 15, v74
	v_and_b32_e32 v70, 0xffffff80, v66
	v_bfe_u32 v67, v66, 4, 2
	v_lshl_add_u64 v[68:69], s[58:59], 0, v[64:65]
	v_ashrrev_i32_e32 v71, 31, v70
	v_or_b32_e32 v90, 16, v84
	v_lshl_add_u64 v[68:69], v[70:71], 1, v[68:69]
	v_lshlrev_b32_e32 v64, 4, v67
	v_ashrrev_i32_e32 v85, 31, v84
	v_ashrrev_i32_e32 v91, 31, v90
	v_lshl_add_u64 v[88:89], v[68:69], 0, v[64:65]
	v_lshlrev_b64 v[68:69], 12, v[84:85]
	v_lshlrev_b64 v[90:91], 12, v[90:91]
	v_lshl_add_u64 v[116:117], v[88:89], 0, v[68:69]
	v_lshl_add_u64 v[120:121], v[88:89], 0, v[90:91]
	s_barrier
	s_waitcnt vmcnt(0)
	v_mov_b32_e32 v68, v148
	v_mov_b32_e32 v69, v149
	v_mov_b32_e32 v70, v150
	v_mov_b32_e32 v71, v151
	v_mov_b32_e32 v76, v152
	v_mov_b32_e32 v77, v153
	v_mov_b32_e32 v78, v154
	v_mov_b32_e32 v79, v155
	v_mov_b32_e32 v92, v156
	v_mov_b32_e32 v93, v157
	v_mov_b32_e32 v94, v158
	v_mov_b32_e32 v95, v159
	v_mov_b32_e32 v96, v160
	v_mov_b32_e32 v97, v161
	v_mov_b32_e32 v98, v162
	v_mov_b32_e32 v99, v163
	v_ashrrev_i32_e32 v75, 2, v66
	v_and_b32_e32 v64, 0x4f, v66
	v_lshlrev_b32_e32 v64, 2, v64
	s_mov_b64 s[20:21], -1
	s_mov_b32 s69, 0
	v_mfma_f32_16x16x32_bf16 v[80:83], v[68:71], v[0:3], 0
	v_mfma_f32_16x16x32_bf16 v[84:87], v[68:71], v[56:59], 0
	v_mfma_f32_16x16x32_bf16 v[88:91], v[68:71], v[24:27], 0
	v_mfma_f32_16x16x32_bf16 v[68:71], v[68:71], v[44:47], 0
	v_mfma_f32_16x16x32_bf16 v[100:103], v[92:95], v[0:3], 0
	v_mfma_f32_16x16x32_bf16 v[104:107], v[92:95], v[56:59], 0
	v_mfma_f32_16x16x32_bf16 v[108:111], v[92:95], v[24:27], 0
	v_mfma_f32_16x16x32_bf16 v[80:83], v[76:79], v[4:7], v[80:83]
	v_mfma_f32_16x16x32_bf16 v[84:87], v[76:79], v[16:19], v[84:87]
	v_mfma_f32_16x16x32_bf16 v[88:91], v[76:79], v[28:31], v[88:91]
	v_mfma_f32_16x16x32_bf16 v[68:71], v[76:79], v[48:51], v[68:71]
	v_mfma_f32_16x16x32_bf16 v[76:79], v[96:99], v[4:7], v[100:103]
	v_mfma_f32_16x16x32_bf16 v[100:103], v[96:99], v[16:19], v[104:107]
	v_mfma_f32_16x16x32_bf16 v[104:107], v[96:99], v[28:31], v[108:111]
	s_nop 2
	s_nop 1
	v_mov_b32_e32 v108, v164
	v_mov_b32_e32 v109, v165
	v_mov_b32_e32 v110, v166
	v_mov_b32_e32 v111, v167
	v_mov_b32_e32 v112, v168
	v_mov_b32_e32 v113, v169
	v_mov_b32_e32 v114, v170
	v_mov_b32_e32 v115, v171
	v_mov_b32_e32 v116, v172
	v_mov_b32_e32 v117, v173
	v_mov_b32_e32 v118, v174
	v_mov_b32_e32 v119, v175
	s_nop 1
	v_mfma_f32_16x16x32_bf16 v[80:83], v[108:111], v[8:11], v[80:83]
	v_mfma_f32_16x16x32_bf16 v[84:87], v[108:111], v[20:23], v[84:87]
	v_mfma_f32_16x16x32_bf16 v[88:91], v[108:111], v[32:35], v[88:91]
	v_mfma_f32_16x16x32_bf16 v[68:71], v[108:111], v[52:55], v[68:71]
	s_nop 3
	v_mov_b32_e32 v108, v178
	v_mov_b32_e32 v109, v179
	v_mov_b32_e32 v110, v180
	v_mov_b32_e32 v111, v181
	v_add_u32_e32 v184, s90, v72
	v_min_u32_e32 v184, s68, v184
	v_lshrrev_b32_e32 v185, 3, v184
	v_lshlrev_b32_e32 v185, 17, v185
	v_and_b32_e32 v184, 7, v184
	v_lshl_or_b32 v184, v184, 9, v185
	v_mov_b32_e32 v185, 0
	v_lshl_add_u64 v[184:185], v[182:183], 0, v[184:185]
	v_mov_b32_e32 v186, 0x10000
	v_mov_b32_e32 v187, 0
	v_lshl_add_u64 v[186:187], v[184:185], 0, v[186:187]
	global_load_dwordx4 v[148:151], v[184:185], off
	global_load_dwordx4 v[152:155], v[184:185], off offset:64
	global_load_dwordx4 v[156:159], v[186:187], off
	global_load_dwordx4 v[160:163], v[186:187], off offset:64
	global_load_dwordx4 v[164:167], v[184:185], off offset:128
	global_load_dwordx4 v[168:171], v[184:185], off offset:192
	global_load_dwordx4 v[172:175], v[186:187], off offset:128
	global_load_dwordx4 v[178:181], v[186:187], off offset:192
	s_nop 1
	v_mfma_f32_16x16x32_bf16 v[80:83], v[112:115], v[12:15], v[80:83]
	v_mfma_f32_16x16x32_bf16 v[84:87], v[112:115], v[40:43], v[84:87]
	v_mfma_f32_16x16x32_bf16 v[88:91], v[112:115], v[36:39], v[88:91]
	v_mfma_f32_16x16x32_bf16 v[68:71], v[112:115], v[60:63], v[68:71]
	v_and_b32_e32 v112, 0xfffffe0, v75
	v_lshl_or_b32 v67, v67, 2, v112
	v_mul_lo_u32 v67, v67, s2
	v_add3_u32 v64, v146, v67, v64
	v_add_u32_e32 v67, 0x400, v64
	s_nop 0
	ds_write2_b32 v64, v80, v84 offset1:16
	ds_write2_b32 v64, v81, v85 offset0:132 offset1:148
	ds_write2_b32 v67, v82, v86 offset0:8 offset1:24
	ds_write2_b32 v67, v83, v87 offset0:140 offset1:156
	ds_write2_b32 v64, v88, v68 offset0:32 offset1:48
	v_mfma_f32_16x16x32_bf16 v[80:83], v[92:95], v[44:47], 0
	ds_write2_b32 v64, v89, v69 offset0:164 offset1:180
	ds_write2_b32 v67, v90, v70 offset0:40 offset1:56
	ds_write2_b32 v67, v91, v71 offset0:172 offset1:188
	v_add_u32_e32 v67, 0x2000, v64
	v_add_u32_e32 v64, 0x2400, v64
	v_mfma_f32_16x16x32_bf16 v[68:71], v[96:99], v[48:51], v[80:83]
	v_mfma_f32_16x16x32_bf16 v[76:79], v[116:119], v[8:11], v[76:79]
	v_mfma_f32_16x16x32_bf16 v[100:103], v[116:119], v[20:23], v[100:103]
	v_mfma_f32_16x16x32_bf16 v[104:107], v[116:119], v[32:35], v[104:107]
	v_mfma_f32_16x16x32_bf16 v[68:71], v[116:119], v[52:55], v[68:71]
	v_mfma_f32_16x16x32_bf16 v[76:79], v[108:111], v[12:15], v[76:79]
	v_mfma_f32_16x16x32_bf16 v[100:103], v[108:111], v[40:43], v[100:103]
	s_nop 7
	ds_write2_b32 v67, v76, v100 offset0:64 offset1:80
	ds_write2_b32 v67, v77, v101 offset0:196 offset1:212
	v_mfma_f32_16x16x32_bf16 v[104:107], v[108:111], v[36:39], v[104:107]
	ds_write2_b32 v64, v78, v102 offset0:72 offset1:88
	ds_write2_b32 v64, v79, v103 offset0:204 offset1:220
	v_mfma_f32_16x16x32_bf16 v[68:71], v[108:111], v[60:63], v[68:71]
	s_nop 7
	ds_write2_b32 v67, v104, v68 offset0:96 offset1:112
	ds_write2_b32 v67, v105, v69 offset0:228 offset1:244
	ds_write2_b32 v64, v106, v70 offset0:104 offset1:120
	ds_write2_b32 v64, v107, v71 offset0:236 offset1:252
	v_and_b32_e32 v69, 7, v66
	v_lshlrev_b32_e32 v70, 1, v69
	v_ashrrev_i32_e32 v64, 3, v66
	v_lshlrev_b32_e32 v67, 4, v69
	v_lshl_add_u32 v68, v69, 6, v146
	v_cmp_eq_u32_e64 s[0:1], 0, v69
	v_cmp_eq_u32_e64 s[4:5], 1, v69
	v_cmp_eq_u32_e64 s[6:7], 2, v69
	v_cmp_eq_u32_e64 s[8:9], 3, v69
	v_cmp_eq_u32_e64 s[10:11], 4, v69
	v_cmp_eq_u32_e64 s[12:13], 5, v69
	v_cmp_eq_u32_e64 s[14:15], 6, v69
	v_cmp_eq_u32_e64 s[16:17], 7, v69
	v_lshlrev_b32_e32 v69, 2, v70
	s_waitcnt lgkmcnt(0)
	s_barrier
